# indexer unmasked trip loop re-emitted with fine-grained MFMA/VALU interleave and in-place K refills (list-scheduled), on top of v36
# speedup vs baseline: 1.0090x; 1.0090x over previous
.LBB0_708:
	s_mov_b32 s0, 0x20000
	s_add_i32 s52, s52, 16
	s_cmp_ge_i32 s52, s9
	v_add_u32_e32 v195, v201, v142
	v_add_u32_e32 v196, v202, v203
	s_waitcnt vmcnt(8)
	v_mfma_f32_16x16x32_bf16 v[114:117], v[134:137], v[66:69], 0
	v_mfma_f32_16x16x32_bf16 v[114:117], v[130:133], v[70:73], v[114:117]
	v_mfma_f32_16x16x32_bf16 v[74:77], v[134:137], v[2:5], 0
	v_mfma_f32_16x16x32_bf16 v[74:77], v[130:133], v[34:37], v[74:77]
	v_mfma_f32_16x16x32_bf16 v[78:81], v[134:137], v[6:9], 0
	v_mfma_f32_16x16x32_bf16 v[78:81], v[130:133], v[38:41], v[78:81]
	v_mfma_f32_16x16x32_bf16 v[82:85], v[134:137], v[10:13], 0
	v_mfma_f32_16x16x32_bf16 v[82:85], v[130:133], v[42:45], v[82:85]
	v_mfma_f32_16x16x32_bf16 v[86:89], v[134:137], v[14:17], 0
	v_mfma_f32_16x16x32_bf16 v[86:89], v[130:133], v[46:49], v[86:89]
	v_mfma_f32_16x16x32_bf16 v[98:101], v[134:137], v[18:21], 0
	v_mfma_f32_16x16x32_bf16 v[98:101], v[130:133], v[50:53], v[98:101]
	v_mfma_f32_16x16x32_bf16 v[102:105], v[134:137], v[22:25], 0
	v_fma_f32 v114, v156, |v74|, v114
	v_fma_f32 v115, v156, |v75|, v115
	v_fma_f32 v116, v156, |v76|, v116
	v_fma_f32 v117, v156, |v77|, v117
	v_fma_f32 v114, v158, |v78|, v114
	v_mfma_f32_16x16x32_bf16 v[102:105], v[130:133], v[54:57], v[102:105]
	v_fma_f32 v115, v158, |v79|, v115
	v_fma_f32 v116, v158, |v80|, v116
	v_fma_f32 v117, v158, |v81|, v117
	v_fma_f32 v114, v160, |v82|, v114
	v_fma_f32 v115, v160, |v83|, v115
	v_mfma_f32_16x16x32_bf16 v[224:227], v[134:137], v[26:29], 0
	v_fma_f32 v116, v160, |v84|, v116
	v_fma_f32 v117, v160, |v85|, v117
	v_fma_f32 v114, v162, |v86|, v114
	v_fma_f32 v115, v162, |v87|, v115
	v_fma_f32 v116, v162, |v88|, v116
	v_mfma_f32_16x16x32_bf16 v[224:227], v[130:133], v[58:61], v[224:227]
	v_fma_f32 v117, v162, |v89|, v117
	v_fma_f32 v114, v164, |v98|, v114
	v_fma_f32 v115, v164, |v99|, v115
	v_fma_f32 v116, v164, |v100|, v116
	v_fma_f32 v117, v164, |v101|, v117
	v_mfma_f32_16x16x32_bf16 v[228:231], v[134:137], v[30:33], 0
	v_fma_f32 v114, v166, |v102|, v114
	v_fma_f32 v115, v166, |v103|, v115
	v_fma_f32 v116, v166, |v104|, v116
	v_fma_f32 v117, v166, |v105|, v117
	v_fma_f32 v114, v168, |v224|, v114
	v_mfma_f32_16x16x32_bf16 v[228:231], v[130:133], v[62:65], v[228:231]
	v_fma_f32 v115, v168, |v225|, v115
	v_fma_f32 v116, v168, |v226|, v116
	v_fma_f32 v117, v168, |v227|, v117
	v_add_u32_e32 v194, -48, v157
	v_min_u32_e32 v194, 0x1fff, v194
	v_lshlrev_b32_e32 v140, 7, v194
	v_lshl_add_u64 v[192:193], v[172:173], 0, v[140:141]
	global_load_dwordx4 v[134:137], v[192:193], off
	global_load_dwordx4 v[130:133], v[192:193], off offset:1024
	s_waitcnt vmcnt(8)
	v_mfma_f32_16x16x32_bf16 v[118:121], v[126:129], v[66:69], 0
	v_fma_f32 v114, v170, |v228|, v114
	v_fma_f32 v115, v170, |v229|, v115
	v_fma_f32 v116, v170, |v230|, v116
	v_fma_f32 v117, v170, |v231|, v117
	v_cvt_pk_f16_f32 v184, v114, v115
	v_mfma_f32_16x16x32_bf16 v[118:121], v[122:125], v[70:73], v[118:121]
	v_cvt_pk_f16_f32 v185, v116, v117
	v_pk_ashrrev_i16 v186, 15, v184 op_sel_hi:[0,1]
	v_bitop3_b32 v176, v186, v184, s3 bitop3:0x36
	v_pk_ashrrev_i16 v186, 15, v185 op_sel_hi:[0,1]
	v_bitop3_b32 v177, v186, v185, s3 bitop3:0x36
	v_mfma_f32_16x16x32_bf16 v[74:77], v[126:129], v[2:5], 0
	v_bfe_u32 v188, v176, 7, 9
	v_lshrrev_b32_e32 v189, 23, v176
	v_bfe_u32 v190, v177, 7, 9
	v_lshrrev_b32_e32 v191, 23, v177
	v_lshl_add_u32 v188, v188, 2, v143
	v_mfma_f32_16x16x32_bf16 v[74:77], v[122:125], v[34:37], v[74:77]
	v_lshl_add_u32 v189, v189, 2, v143
	v_lshl_add_u32 v190, v190, 2, v143
	v_lshl_add_u32 v191, v191, 2, v143
	ds_add_u32 v188, v206
	ds_add_u32 v189, v206
	v_mfma_f32_16x16x32_bf16 v[78:81], v[126:129], v[6:9], 0
	ds_add_u32 v190, v206
	ds_add_u32 v191, v206
	v_mfma_f32_16x16x32_bf16 v[78:81], v[122:125], v[38:41], v[78:81]
	v_fma_f32 v118, v156, |v74|, v118
	v_fma_f32 v119, v156, |v75|, v119
	v_fma_f32 v120, v156, |v76|, v120
	v_fma_f32 v121, v156, |v77|, v121
	v_mfma_f32_16x16x32_bf16 v[82:85], v[126:129], v[10:13], 0
	v_mfma_f32_16x16x32_bf16 v[82:85], v[122:125], v[42:45], v[82:85]
	v_mfma_f32_16x16x32_bf16 v[86:89], v[126:129], v[14:17], 0
	v_mfma_f32_16x16x32_bf16 v[86:89], v[122:125], v[46:49], v[86:89]
	v_mfma_f32_16x16x32_bf16 v[98:101], v[126:129], v[18:21], 0
	v_fma_f32 v118, v158, |v78|, v118
	v_fma_f32 v119, v158, |v79|, v119
	v_fma_f32 v120, v158, |v80|, v120
	v_fma_f32 v121, v158, |v81|, v121
	v_mfma_f32_16x16x32_bf16 v[98:101], v[122:125], v[50:53], v[98:101]
	v_mfma_f32_16x16x32_bf16 v[102:105], v[126:129], v[22:25], 0
	v_fma_f32 v118, v160, |v82|, v118
	v_fma_f32 v119, v160, |v83|, v119
	v_fma_f32 v120, v160, |v84|, v120
	v_fma_f32 v121, v160, |v85|, v121
	v_fma_f32 v118, v162, |v86|, v118
	v_mfma_f32_16x16x32_bf16 v[102:105], v[122:125], v[54:57], v[102:105]
	v_fma_f32 v119, v162, |v87|, v119
	v_fma_f32 v120, v162, |v88|, v120
	v_fma_f32 v121, v162, |v89|, v121
	v_fma_f32 v118, v164, |v98|, v118
	v_fma_f32 v119, v164, |v99|, v119
	v_mfma_f32_16x16x32_bf16 v[224:227], v[126:129], v[26:29], 0
	v_fma_f32 v120, v164, |v100|, v120
	v_fma_f32 v121, v164, |v101|, v121
	v_mfma_f32_16x16x32_bf16 v[224:227], v[122:125], v[58:61], v[224:227]
	v_fma_f32 v118, v166, |v102|, v118
	v_fma_f32 v119, v166, |v103|, v119
	v_fma_f32 v120, v166, |v104|, v120
	v_fma_f32 v121, v166, |v105|, v121
	v_mfma_f32_16x16x32_bf16 v[228:231], v[126:129], v[30:33], 0
	v_mfma_f32_16x16x32_bf16 v[228:231], v[122:125], v[62:65], v[228:231]
	v_add_u32_e32 v194, -32, v157
	v_min_u32_e32 v194, 0x1fff, v194
	v_lshlrev_b32_e32 v140, 7, v194
	v_lshl_add_u64 v[192:193], v[172:173], 0, v[140:141]
	global_load_dwordx4 v[126:129], v[192:193], off
	global_load_dwordx4 v[122:125], v[192:193], off offset:1024
	s_waitcnt vmcnt(8)
	v_mfma_f32_16x16x32_bf16 v[114:117], v[110:113], v[66:69], 0
	v_fma_f32 v118, v168, |v224|, v118
	v_fma_f32 v119, v168, |v225|, v119
	v_fma_f32 v120, v168, |v226|, v120
	v_fma_f32 v121, v168, |v227|, v121
	v_fma_f32 v118, v170, |v228|, v118
	v_mfma_f32_16x16x32_bf16 v[114:117], v[106:109], v[70:73], v[114:117]
	v_fma_f32 v119, v170, |v229|, v119
	v_fma_f32 v120, v170, |v230|, v120
	v_fma_f32 v121, v170, |v231|, v121
	v_cvt_pk_f16_f32 v184, v118, v119
	v_cvt_pk_f16_f32 v185, v120, v121
	v_mfma_f32_16x16x32_bf16 v[74:77], v[110:113], v[2:5], 0
	v_pk_ashrrev_i16 v186, 15, v184 op_sel_hi:[0,1]
	v_bitop3_b32 v178, v186, v184, s3 bitop3:0x36
	v_pk_ashrrev_i16 v186, 15, v185 op_sel_hi:[0,1]
	v_bitop3_b32 v179, v186, v185, s3 bitop3:0x36
	v_bfe_u32 v188, v178, 7, 9
	v_mfma_f32_16x16x32_bf16 v[74:77], v[106:109], v[34:37], v[74:77]
	v_lshrrev_b32_e32 v189, 23, v178
	v_bfe_u32 v190, v179, 7, 9
	v_lshrrev_b32_e32 v191, 23, v179
	v_lshl_add_u32 v188, v188, 2, v143
	v_lshl_add_u32 v189, v189, 2, v143
	v_mfma_f32_16x16x32_bf16 v[78:81], v[110:113], v[6:9], 0
	v_lshl_add_u32 v190, v190, 2, v143
	v_lshl_add_u32 v191, v191, 2, v143
	ds_add_u32 v188, v206
	ds_add_u32 v189, v206
	ds_add_u32 v190, v206
	v_mfma_f32_16x16x32_bf16 v[78:81], v[106:109], v[38:41], v[78:81]
	ds_add_u32 v191, v206
	v_fma_f32 v114, v156, |v74|, v114
	v_fma_f32 v115, v156, |v75|, v115
	v_fma_f32 v116, v156, |v76|, v116
	v_fma_f32 v117, v156, |v77|, v117
	v_mfma_f32_16x16x32_bf16 v[82:85], v[110:113], v[10:13], 0
	v_mfma_f32_16x16x32_bf16 v[82:85], v[106:109], v[42:45], v[82:85]
	v_mfma_f32_16x16x32_bf16 v[86:89], v[110:113], v[14:17], 0
	v_mfma_f32_16x16x32_bf16 v[86:89], v[106:109], v[46:49], v[86:89]
	v_fma_f32 v114, v158, |v78|, v114
	v_fma_f32 v115, v158, |v79|, v115
	v_fma_f32 v116, v158, |v80|, v116
	v_fma_f32 v117, v158, |v81|, v117
	v_mfma_f32_16x16x32_bf16 v[98:101], v[110:113], v[18:21], 0
	v_mfma_f32_16x16x32_bf16 v[98:101], v[106:109], v[50:53], v[98:101]
	v_mfma_f32_16x16x32_bf16 v[102:105], v[110:113], v[22:25], 0
	v_fma_f32 v114, v160, |v82|, v114
	v_fma_f32 v115, v160, |v83|, v115
	v_fma_f32 v116, v160, |v84|, v116
	v_fma_f32 v117, v160, |v85|, v117
	v_fma_f32 v114, v162, |v86|, v114
	v_mfma_f32_16x16x32_bf16 v[102:105], v[106:109], v[54:57], v[102:105]
	v_fma_f32 v115, v162, |v87|, v115
	v_fma_f32 v116, v162, |v88|, v116
	v_fma_f32 v117, v162, |v89|, v117
	v_fma_f32 v114, v164, |v98|, v114
	v_fma_f32 v115, v164, |v99|, v115
	v_mfma_f32_16x16x32_bf16 v[224:227], v[110:113], v[26:29], 0
	v_fma_f32 v116, v164, |v100|, v116
	v_fma_f32 v117, v164, |v101|, v117
	v_mfma_f32_16x16x32_bf16 v[224:227], v[106:109], v[58:61], v[224:227]
	v_fma_f32 v114, v166, |v102|, v114
	v_fma_f32 v115, v166, |v103|, v115
	v_fma_f32 v116, v166, |v104|, v116
	v_fma_f32 v117, v166, |v105|, v117
	v_mfma_f32_16x16x32_bf16 v[228:231], v[110:113], v[30:33], 0
	v_mfma_f32_16x16x32_bf16 v[228:231], v[106:109], v[62:65], v[228:231]
	v_add_u32_e32 v194, -16, v157
	v_min_u32_e32 v194, 0x1fff, v194
	v_lshlrev_b32_e32 v140, 7, v194
	v_lshl_add_u64 v[192:193], v[172:173], 0, v[140:141]
	global_load_dwordx4 v[110:113], v[192:193], off
	global_load_dwordx4 v[106:109], v[192:193], off offset:1024
	s_waitcnt vmcnt(8)
	v_mfma_f32_16x16x32_bf16 v[118:121], v[94:97], v[66:69], 0
	v_fma_f32 v114, v168, |v224|, v114
	v_fma_f32 v115, v168, |v225|, v115
	v_fma_f32 v116, v168, |v226|, v116
	v_fma_f32 v117, v168, |v227|, v117
	v_fma_f32 v114, v170, |v228|, v114
	v_mfma_f32_16x16x32_bf16 v[118:121], v[90:93], v[70:73], v[118:121]
	v_fma_f32 v115, v170, |v229|, v115
	v_fma_f32 v116, v170, |v230|, v116
	v_fma_f32 v117, v170, |v231|, v117
	v_cvt_pk_f16_f32 v184, v114, v115
	v_cvt_pk_f16_f32 v185, v116, v117
	v_mfma_f32_16x16x32_bf16 v[74:77], v[94:97], v[2:5], 0
	v_pk_ashrrev_i16 v186, 15, v184 op_sel_hi:[0,1]
	v_bitop3_b32 v180, v186, v184, s3 bitop3:0x36
	v_pk_ashrrev_i16 v186, 15, v185 op_sel_hi:[0,1]
	v_bitop3_b32 v181, v186, v185, s3 bitop3:0x36
	v_bfe_u32 v188, v180, 7, 9
	v_mfma_f32_16x16x32_bf16 v[74:77], v[90:93], v[34:37], v[74:77]
	v_lshrrev_b32_e32 v189, 23, v180
	v_bfe_u32 v190, v181, 7, 9
	v_lshrrev_b32_e32 v191, 23, v181
	v_lshl_add_u32 v188, v188, 2, v143
	v_lshl_add_u32 v189, v189, 2, v143
	v_mfma_f32_16x16x32_bf16 v[78:81], v[94:97], v[6:9], 0
	v_lshl_add_u32 v190, v190, 2, v143
	v_lshl_add_u32 v191, v191, 2, v143
	ds_add_u32 v188, v206
	ds_add_u32 v189, v206
	ds_add_u32 v190, v206
	v_mfma_f32_16x16x32_bf16 v[78:81], v[90:93], v[38:41], v[78:81]
	ds_add_u32 v191, v206
	v_fma_f32 v118, v156, |v74|, v118
	v_fma_f32 v119, v156, |v75|, v119
	v_fma_f32 v120, v156, |v76|, v120
	v_fma_f32 v121, v156, |v77|, v121
	v_mfma_f32_16x16x32_bf16 v[82:85], v[94:97], v[10:13], 0
	v_mfma_f32_16x16x32_bf16 v[82:85], v[90:93], v[42:45], v[82:85]
	v_mfma_f32_16x16x32_bf16 v[86:89], v[94:97], v[14:17], 0
	v_mfma_f32_16x16x32_bf16 v[86:89], v[90:93], v[46:49], v[86:89]
	v_fma_f32 v118, v158, |v78|, v118
	v_fma_f32 v119, v158, |v79|, v119
	v_fma_f32 v120, v158, |v80|, v120
	v_fma_f32 v121, v158, |v81|, v121
	v_mfma_f32_16x16x32_bf16 v[98:101], v[94:97], v[18:21], 0
	v_mfma_f32_16x16x32_bf16 v[98:101], v[90:93], v[50:53], v[98:101]
	v_mfma_f32_16x16x32_bf16 v[102:105], v[94:97], v[22:25], 0
	v_fma_f32 v118, v160, |v82|, v118
	v_fma_f32 v119, v160, |v83|, v119
	v_fma_f32 v120, v160, |v84|, v120
	v_fma_f32 v121, v160, |v85|, v121
	v_fma_f32 v118, v162, |v86|, v118
	v_mfma_f32_16x16x32_bf16 v[102:105], v[90:93], v[54:57], v[102:105]
	v_fma_f32 v119, v162, |v87|, v119
	v_fma_f32 v120, v162, |v88|, v120
	v_fma_f32 v121, v162, |v89|, v121
	v_fma_f32 v118, v164, |v98|, v118
	v_fma_f32 v119, v164, |v99|, v119
	v_mfma_f32_16x16x32_bf16 v[224:227], v[94:97], v[26:29], 0
	v_fma_f32 v120, v164, |v100|, v120
	v_fma_f32 v121, v164, |v101|, v121
	v_mfma_f32_16x16x32_bf16 v[224:227], v[90:93], v[58:61], v[224:227]
	v_fma_f32 v118, v166, |v102|, v118
	v_fma_f32 v119, v166, |v103|, v119
	v_fma_f32 v120, v166, |v104|, v120
	v_fma_f32 v121, v166, |v105|, v121
	v_mfma_f32_16x16x32_bf16 v[228:231], v[94:97], v[30:33], 0
	v_mfma_f32_16x16x32_bf16 v[228:231], v[90:93], v[62:65], v[228:231]
	s_nop 2
	v_fma_f32 v118, v168, |v224|, v118
	v_fma_f32 v119, v168, |v225|, v119
	v_fma_f32 v120, v168, |v226|, v120
	v_fma_f32 v121, v168, |v227|, v121
	s_nop 1
	v_fma_f32 v118, v170, |v228|, v118
	v_fma_f32 v119, v170, |v229|, v119
	v_fma_f32 v120, v170, |v230|, v120
	v_fma_f32 v121, v170, |v231|, v121
	v_cvt_pk_f16_f32 v184, v118, v119
	v_cvt_pk_f16_f32 v185, v120, v121
	v_pk_ashrrev_i16 v186, 15, v184 op_sel_hi:[0,1]
	v_bitop3_b32 v182, v186, v184, s3 bitop3:0x36
	v_pk_ashrrev_i16 v186, 15, v185 op_sel_hi:[0,1]
	v_bitop3_b32 v183, v186, v185, s3 bitop3:0x36
	v_bfe_u32 v188, v182, 7, 9
	v_lshrrev_b32_e32 v189, 23, v182
	v_bfe_u32 v190, v183, 7, 9
	v_lshrrev_b32_e32 v191, 23, v183
	v_lshl_add_u32 v188, v188, 2, v143
	v_lshl_add_u32 v189, v189, 2, v143
	v_lshl_add_u32 v190, v190, 2, v143
	v_lshl_add_u32 v191, v191, 2, v143
	ds_add_u32 v188, v206
	ds_add_u32 v189, v206
	ds_add_u32 v190, v206
	ds_add_u32 v191, v206
	v_mov_b32_e32 v194, v157
	v_min_u32_e32 v194, 0x1fff, v194
	v_lshlrev_b32_e32 v140, 7, v194
	v_lshl_add_u64 v[192:193], v[172:173], 0, v[140:141]
	global_load_dwordx4 v[94:97], v[192:193], off
	global_load_dwordx4 v[90:93], v[192:193], off offset:1024
	v_add_u32_e32 v157, 0x100, v157
	ds_write2_b64 v195, v[176:177], v[178:179] offset1:4
	ds_write2_b64 v195, v[180:181], v[182:183] offset0:8 offset1:12
	s_waitcnt lgkmcnt(0)
	ds_read_b128 v[232:235], v196
	ds_read_b128 v[236:239], v196 offset:1152
	s_waitcnt lgkmcnt(1)
	global_store_dwordx4 v[174:175], v[232:235], off
	v_add_co_u32_e32 v198, vcc, s0, v174
	s_nop 1
	v_addc_co_u32_e32 v199, vcc, 0, v175, vcc
	s_waitcnt lgkmcnt(0)
	global_store_dwordx4 v[198:199], v[236:239], off
	v_lshl_add_u64 v[174:175], v[174:175], 0, s[14:15]
	s_cbranch_scc0 .LBB0_708
	s_waitcnt vmcnt(2)
	v_mov_b64_e32 v[118:119], v[134:135]
	v_mov_b64_e32 v[120:121], v[136:137]
	v_mov_b64_e32 v[114:115], v[130:131]
	v_mov_b64_e32 v[116:117], v[132:133]
	v_mov_b64_e32 v[102:103], v[126:127]
	v_mov_b64_e32 v[104:105], v[128:129]
	v_mov_b64_e32 v[98:99], v[122:123]
	v_mov_b64_e32 v[100:101], v[124:125]
	v_mov_b64_e32 v[86:87], v[110:111]
	v_mov_b64_e32 v[88:89], v[112:113]
	v_mov_b64_e32 v[82:83], v[106:107]
	v_mov_b64_e32 v[84:85], v[108:109]
	v_mov_b64_e32 v[78:79], v[94:95]
	v_mov_b64_e32 v[80:81], v[96:97]
	v_mov_b64_e32 v[74:75], v[90:91]
	v_mov_b64_e32 v[76:77], v[92:93]
	s_branch .LBB0_710
